# P7: static s_setprio 1 for waves 4-7 over the attention phase
# speedup vs baseline: 1.0028x; 1.0026x over previous
.LBB0_1715:
	s_cmp_lt_i32 s46, 8
	s_cselect_b64 s[6:7], -1, 0
	s_and_b64 s[8:9], s[6:7], s[4:5]
	s_andn2_b64 vcc, exec, s[8:9]
	s_cbranch_vccnz .LBB0_1746
	s_mov_b64 s[4:5], s[0:1]
	v_mov_b32_e32 v2, v0
	s_cmpk_gt_i32 s2, 0x1ff
	s_cbranch_scc1 .LBB0_1746
	s_cmp_lt_u32 s52, 4
	s_cbranch_scc1 .Lp7prio
	s_setprio 1
.Lp7prio:
	v_lshrrev_b32_e32 v1, 4, v0
	v_lshrrev_b32_e32 v9, 3, v0
	v_and_b32_e32 v9, 8, v9
	v_or_b32_e32 v15, 32, v1
	v_lshlrev_b32_e32 v5, 3, v0
	v_and_or_b32 v10, v1, 16, v9
	v_and_or_b32 v9, v15, 48, v9
	v_and_b32_e32 v7, 0x78, v5
	v_lshrrev_b32_e32 v11, 5, v0
	v_lshrrev_b32_e32 v10, 1, v10
	v_bfe_u32 v12, v5, 5, 2
	v_bfe_u32 v13, v0, 4, 2
	v_lshrrev_b32_e32 v9, 1, v9
	v_or_b32_e32 v10, v10, v12
	v_and_or_b32 v11, v11, 4, v13
	v_lshlrev_b32_e32 v13, 1, v7
	v_or_b32_e32 v9, v9, v12
	v_lshlrev_b32_e32 v10, 9, v10
	v_lshlrev_b32_e32 v11, 6, v11
	v_and_b32_e32 v14, 48, v13
	v_lshlrev_b32_e32 v9, 9, v9
	v_or3_b32 v10, v10, v11, v14
	v_or3_b32 v9, v9, v11, v14
	v_lshlrev_b32_e32 v11, 4, v0
	v_lshlrev_b32_e32 v14, 1, v0
	v_and_b32_e32 v12, 0xc0, v11
	v_and_b32_e32 v14, 32, v14
	v_and_b32_e32 v5, 0x118, v5
	v_or3_b32 v12, v14, v12, v5
	v_mul_u32_u24_e32 v14, 0x2700, v1
	v_or_b32_e32 v5, v14, v7
	v_bfe_u32 v6, v0, 5, 1
	s_waitcnt vmcnt(23)
	v_lshlrev_b32_e32 v150, 1, v5
	v_lshlrev_b32_e32 v1, 8, v1
	v_and_b32_e32 v5, 0x70, v0
	s_movk_i32 s4, 0x70
	v_bitop3_b32 v16, v13, v1, v5 bitop3:0xde
	v_lshlrev_b32_e32 v1, 8, v15
	v_lshlrev_b32_e32 v15, 4, v6
	v_bitop3_b32 v13, v13, v1, v5 bitop3:0xde
	v_and_b32_e32 v1, 0x70, v11
	v_bitop3_b32 v11, v15, v11, s4 bitop3:0x78
	s_movk_i32 s4, 0x60
	s_waitcnt vmcnt(0)
	v_bitop3_b32 v19, v15, v1, s4 bitop3:0x36
	s_movk_i32 s4, 0x80
	s_add_u32 s10, s44, 0x49098000
	v_and_b32_e32 v146, 31, v2
	v_mov_b32_e32 v149, 0
	v_and_b32_e32 v3, 63, v0
	s_movk_i32 s3, 0xc0
	v_bitop3_b32 v20, v15, v1, s4 bitop3:0x36
	s_movk_i32 s4, 0xa0
	v_lshrrev_b32_e32 v2, 1, v2
	s_addc_u32 s11, s45, 0
	v_and_b32_e32 v4, 31, v0
	v_bitop3_b32 v21, v15, v1, s4 bitop3:0x36
	v_bitop3_b32 v22, v15, v1, s3 bitop3:0x36
	s_movk_i32 s3, 0xe0
	v_cmp_gt_u32_e64 s[4:5], 32, v3
	v_mov_b32_e32 v5, v149
	v_and_b32_e32 v2, 16, v2
	v_mov_b32_e32 v3, v149
	v_and_b32_e32 v8, 0x1c0, v0
	v_bitop3_b32 v17, v15, v1, 32 bitop3:0x36
	v_bitop3_b32 v18, v15, v1, 64 bitop3:0x36
	v_bitop3_b32 v23, v15, v1, s3 bitop3:0x36
	v_lshlrev_b32_e32 v1, 2, v6
	v_lshlrev_b32_e32 v6, 12, v6
	v_mov_b32_e32 v7, v149
	v_lshl_add_u64 v[154:155], s[10:11], 0, v[2:3]
	s_add_i32 s6, 0, 0x10000
	v_lshl_add_u64 v[2:3], s[44:45], 0, v[4:5]
	v_lshl_add_u32 v8, v8, 2, s6
	v_lshl_add_u64 v[2:3], v[2:3], 0, v[6:7]
	s_mov_b64 s[6:7], 0x9aa98000
	v_lshlrev_b32_e32 v148, 10, v4
	v_lshl_add_u64 v[156:157], v[2:3], 0, s[6:7]
	s_add_i32 s6, 0, 0x4000
	v_add_u32_e32 v197, s6, v12
	v_lshl_add_u64 v[2:3], s[44:45], 0, v[148:149]
	s_mov_b64 s[6:7], 0x98a98000
	s_lshl_b32 s3, s52, 5
	v_lshl_add_u32 v5, v4, 8, 0
	v_lshl_add_u64 v[158:159], v[2:3], 0, s[6:7]
	v_and_b32_e32 v2, 15, v0
	v_lshlrev_b32_e32 v3, 1, v14
	v_add_u32_e32 v152, 0x9c000, v150
	v_mov_b32_e32 v151, v149
	v_mov_b32_e32 v153, v149
	s_and_b32 s3, s3, 32
	s_and_b32 s19, s66, 0xffffff80
	s_mov_b32 s13, 0
	v_add_u32_e32 v147, 0, v12
	v_lshl_add_u32 v196, v4, 2, v8
	s_movk_i32 s30, 0x4000
	v_add_u32_e32 v198, v8, v15
	v_lshl_or_b32 v160, v2, 4, v3
	v_mov_b32_e32 v161, v149
	s_mov_b64 s[14:15], 0xa00
	s_mov_b64 s[16:17], 0x800
	s_movk_i32 s31, 0x4e00
	s_mov_b32 s34, 0xff800000
	s_mov_b32 s35, 0x42b504f3
	s_mov_b32 s18, 0x3e0293ee
	s_mov_b32 s36, 0x49308000
	s_mov_b32 s37, 0x493a4000
	s_mov_b32 s38, 0x49440000
	s_mov_b32 s39, 0x494dc000
	s_mov_b64 s[20:21], 0x270000
	s_mov_b32 s40, 0xc3e00000
	s_movk_i32 s41, 0x2000
	s_movk_i32 s42, 0x6000
	v_mov_b32_e32 v149, 0x4e00
	v_add_u32_e32 v199, 0, v10
	v_add_u32_e32 v200, 0, v9
	v_add_u32_e32 v201, 0, v16
	v_add_u32_e32 v202, 0, v13
	v_add_u32_e32 v203, v5, v11
	v_add_u32_e32 v204, v5, v17
	v_add_u32_e32 v205, v5, v18
	v_add_u32_e32 v206, v5, v19
	v_add_u32_e32 v207, v5, v20
	v_add_u32_e32 v208, v5, v21
	v_add_u32_e32 v209, v5, v22
	v_add_u32_e32 v210, v5, v23
	v_mov_b32_e32 v211, 0xf149f2ca
	v_mov_b32_e32 v212, 0x43e00000
	s_mov_b32 s43, s2
	s_branch .LBB0_1719

.LBB0_1746:
	s_setprio 0
	s_cmp_gt_i32 s47, 8
	s_cselect_b64 s[4:5], -1, 0
	s_and_b64 s[6:7], s[8:9], s[4:5]
	s_andn2_b64 vcc, exec, s[6:7]
	s_cbranch_vccnz .LBB0_1796
	s_waitcnt vmcnt(0)
	v_cmp_eq_u32_e32 vcc, 0, v0
	s_waitcnt vmcnt(0) lgkmcnt(0)
	s_barrier
	s_and_saveexec_b64 s[6:7], vcc
	s_cbranch_execz .LBB0_1795
	s_add_i32 s3, 0, 0x23ff0
	v_mov_b32_e32 v1, s3
	s_waitcnt vmcnt(0) expcnt(0) lgkmcnt(0)
	ds_read_b32 v3, v1
	s_add_i32 s3, 0, 0x23ff4
	v_mov_b32_e32 v1, s3
	ds_read_b32 v1, v1
	s_waitcnt lgkmcnt(1)
	v_cmp_ne_u32_e32 vcc, 0, v3
	s_cbranch_vccnz .LBB0_1763
	s_load_dwordx2 s[12:13], s[50:51], 0x4
	s_add_u32 s8, s44, 0x1000
	s_addc_u32 s9, s45, 0
	s_add_u32 s10, s44, 0x1100
	s_addc_u32 s11, s45, 0
	s_waitcnt lgkmcnt(0)
	s_mul_i32 s3, s12, s48
	s_add_u32 s12, s44, 0x1200
	s_mul_i32 s3, s3, s13
	s_addc_u32 s13, s45, 0
	s_add_u32 s14, s44, 0x1300
	s_addc_u32 s15, s45, 0
	s_mov_b32 s22, 1
	v_mov_b32_e32 v17, 0
	s_branch .LBB0_1751
